# speedup vs baseline: 1.1080x; 1.0029x over previous
.LBB2_93:
	ds_read_b128 v[18:21], v125 offset:8192
	ds_read_b128 v[34:37], v125 offset:9216
	v_cvt_pkrtz_f16_f32 v50, v74, v75
	v_cvt_pkrtz_f16_f32 v51, v76, v77
	v_cvt_pkrtz_f16_f32 v52, v82, v83
	v_cvt_pkrtz_f16_f32 v53, v84, v85
	v_cvt_pkrtz_f16_f32 v62, v86, v87
	v_cvt_pkrtz_f16_f32 v63, v88, v89
	v_cvt_pkrtz_f16_f32 v64, v94, v95
	s_waitcnt lgkmcnt(0)
	v_mfma_f32_32x32x16_f16 v[18:33], v[18:21], v[50:53], 0
	v_cvt_pkrtz_f16_f32 v65, v110, v111
	ds_read_b128 v[38:41], v125 offset:10240
	v_cvt_pkrtz_f16_f32 v78, v108, v109
	v_cvt_pkrtz_f16_f32 v79, v106, v107
	v_cvt_pkrtz_f16_f32 v80, v104, v105
	v_cvt_pkrtz_f16_f32 v81, v100, v101
	s_add_i32 s0, 0, 0x1a800
	v_mfma_f32_32x32x16_f16 v[18:33], v[34:37], v[62:65], v[18:33]
	v_lshl_add_u32 v99, v165, 1, s0
	ds_read_b128 v[2:5], v125
	ds_read_b128 v[58:61], v125 offset:1024
	ds_read_b128 v[120:123], v125 offset:2048
	ds_read_b128 v[174:177], v125 offset:3072
	ds_read_b128 v[178:181], v125 offset:4096
	ds_read_b128 v[182:185], v125 offset:5120
	ds_read_b128 v[34:37], v125 offset:11264
	ds_read_b128 v[186:189], v125 offset:6144
	ds_read_b128 v[190:193], v125 offset:7168
	v_cvt_pkrtz_f16_f32 v114, v96, v97
	v_cvt_pkrtz_f16_f32 v115, v92, v93
	s_waitcnt lgkmcnt(0)
	v_mfma_f32_32x32x16_f16 v[18:33], v[38:41], v[78:81], v[18:33]
	ds_read_b128 v[194:197], v99 offset:11648
	ds_read_b128 v[198:201], v99 offset:11936
	ds_read_b128 v[38:41], v125 offset:12288
	v_cvt_pkrtz_f16_f32 v116, v90, v91
	v_cvt_pkrtz_f16_f32 v117, v102, v103
	ds_read_b128 v[202:205], v99 offset:12224
	ds_read_b128 v[206:209], v99 offset:12512
	ds_read_b128 v[210:213], v99 offset:12800
	ds_read_b128 v[54:57], v99 offset:13088
	ds_read_b128 v[70:73], v99 offset:13376
	ds_read_b128 v[66:69], v99 offset:13664
	ds_read_b128 v[214:217], v125 offset:13312
	ds_read_b128 v[218:221], v99 offset:13952
	ds_read_b128 v[222:225], v125 offset:14336
	ds_read_b128 v[226:229], v125 offset:15360
	ds_read_b128 v[230:233], v99 offset:14240
	s_mov_b32 s16, 0xff61b1e6
	s_mov_b32 s17, 0
	v_mfma_f32_32x32x16_f16 v[18:33], v[34:37], v[114:117], v[18:33]
	s_waitcnt lgkmcnt(0)
	v_mfma_f32_32x32x16_f16 v[34:49], v[38:41], v[50:53], 0
	s_nop 9
	v_add_f32_e32 v112, v18, v218
	v_add_f32_e32 v113, v19, v219
	v_add_f32_e32 v159, v20, v220
	v_add_f32_e32 v161, v21, v221
	ds_read_b128 v[18:21], v99 offset:14528
	v_add_f32_e32 v164, v22, v230
	v_add_f32_e32 v165, v23, v231
	v_mfma_f32_32x32x16_f16 v[34:49], v[214:217], v[62:65], v[34:49]
	v_add_f32_e32 v170, v24, v232
	v_add_f32_e32 v173, v25, v233
	ds_read_b128 v[22:25], v99 offset:14816
	s_waitcnt lgkmcnt(0)
	v_add_f32_e32 v26, v26, v18
	v_add_f32_e32 v27, v27, v19
	v_add_f32_e32 v28, v28, v20
	v_add_f32_e32 v29, v29, v21
	v_mfma_f32_32x32x16_f16 v[34:49], v[222:225], v[78:81], v[34:49]
	ds_read_b128 v[18:21], v99 offset:15104
	v_add_f32_e32 v30, v30, v22
	v_add_f32_e32 v31, v31, v23
	v_add_f32_e32 v32, v32, v24
	v_add_f32_e32 v33, v33, v25
	ds_read_b128 v[22:25], v99 offset:15392
	v_mfma_f32_32x32x16_f16 v[34:49], v[226:229], v[114:117], v[34:49]
	v_mfma_f32_32x32x16_f16 v[2:17], v[2:5], v[50:53], 0
	s_waitcnt lgkmcnt(0)
	s_nop 9
	v_add_f32_e32 v34, v34, v18
	v_add_f32_e32 v35, v35, v19
	v_add_f32_e32 v36, v36, v20
	v_add_f32_e32 v37, v37, v21
	ds_read_b128 v[18:21], v99 offset:15680
	v_add_f32_e32 v38, v38, v22
	v_add_f32_e32 v39, v39, v23
	v_add_f32_e32 v40, v40, v24
	v_add_f32_e32 v41, v41, v25
	ds_read_b128 v[22:25], v99 offset:15968
	s_waitcnt lgkmcnt(0)
	v_add_f32_e32 v42, v42, v18
	v_add_f32_e32 v43, v43, v19
	v_add_f32_e32 v44, v44, v20
	v_add_f32_e32 v45, v45, v21
	v_cvt_pkrtz_f16_f32 v18, v112, v113
	v_cvt_pkrtz_f16_f32 v19, v159, v161
	v_cvt_pkrtz_f16_f32 v20, v164, v165
	v_cvt_pkrtz_f16_f32 v21, v170, v173
	ds_write_b128 v166, v[18:21]
	v_cvt_pkrtz_f16_f32 v18, v26, v27
	v_cvt_pkrtz_f16_f32 v19, v28, v29
	v_cvt_pkrtz_f16_f32 v20, v30, v31
	v_cvt_pkrtz_f16_f32 v21, v32, v33
	v_add_f32_e32 v22, v46, v22
	v_add_f32_e32 v23, v47, v23
	v_add_f32_e32 v24, v48, v24
	v_add_f32_e32 v25, v49, v25
	ds_write_b128 v166, v[18:21] offset:32
	v_cvt_pkrtz_f16_f32 v18, v34, v35
	v_cvt_pkrtz_f16_f32 v19, v36, v37
	v_cvt_pkrtz_f16_f32 v20, v38, v39
	v_cvt_pkrtz_f16_f32 v21, v40, v41
	ds_write_b128 v166, v[18:21] offset:64
	v_cvt_pkrtz_f16_f32 v18, v42, v43
	v_cvt_pkrtz_f16_f32 v19, v44, v45
	v_cvt_pkrtz_f16_f32 v20, v22, v23
	v_cvt_pkrtz_f16_f32 v21, v24, v25
	ds_write_b128 v166, v[18:21] offset:96
	ds_read_b128 v[18:21], v125 offset:16384
	ds_read_b128 v[22:25], v125 offset:17408
	s_waitcnt lgkmcnt(0)
	v_mfma_f32_32x32x16_f16 v[30:45], v[50:53], v[18:21], 0
	v_add_u32_e32 v112, v167, v162
	v_add_u32_e32 v159, v171, v172
	v_mfma_f32_32x32x16_f16 v[2:17], v[58:61], v[62:65], v[2:17]
	v_mfma_f32_32x32x16_f16 v[30:45], v[62:65], v[22:25], v[30:45]
	ds_read_b128 v[18:21], v125 offset:18432
	ds_read_b128 v[22:25], v125 offset:19456
	v_mfma_f32_32x32x16_f16 v[2:17], v[120:123], v[78:81], v[2:17]
	s_waitcnt lgkmcnt(0)
	v_mfma_f32_32x32x16_f16 v[30:45], v[78:81], v[18:21], v[30:45]
	v_add3_u32 v18, s0, v168, v160
	ds_read_b32 v46, v18 offset:16256
	v_mfma_f32_32x32x16_f16 v[2:17], v[174:177], v[114:117], v[2:17]
	v_mfma_f32_32x32x16_f16 v[30:45], v[114:117], v[22:25], v[30:45]
	s_nop 10
	v_fmamk_f32 v58, v194, 0x3e38aa3b, v2
	v_fmamk_f32 v59, v195, 0x3e38aa3b, v3
	v_fmamk_f32 v99, v198, 0x3e38aa3b, v6
	v_fmamk_f32 v113, v202, 0x3e38aa3b, v10
	v_fmamk_f32 v120, v203, 0x3e38aa3b, v11
	v_fmamk_f32 v121, v204, 0x3e38aa3b, v12
	v_fmamk_f32 v122, v205, 0x3e38aa3b, v13
	s_waitcnt lgkmcnt(0)
	v_add_f32_e32 v2, v46, v30
	v_add_f32_e32 v3, v46, v31
	v_add_f32_e32 v47, v46, v32
	v_add_f32_e32 v48, v46, v33
	v_add_f32_e32 v49, v46, v34
	v_add_f32_e32 v60, v46, v35
	v_add_f32_e32 v61, v46, v36
	v_add_f32_e32 v37, v46, v37
	v_add_f32_e32 v38, v46, v38
	v_add_f32_e32 v39, v46, v39
	v_add_f32_e32 v40, v46, v40
	v_add_f32_e32 v41, v46, v41
	v_add_f32_e32 v42, v46, v42
	v_add_f32_e32 v43, v46, v43
	v_add_f32_e32 v44, v46, v44
	v_add_f32_e32 v45, v46, v45
	v_cvt_pkrtz_f16_f32 v34, v2, v3
	v_cvt_pkrtz_f16_f32 v35, v47, v48
	v_cvt_pkrtz_f16_f32 v36, v49, v60
	v_cvt_pkrtz_f16_f32 v37, v61, v37
	ds_write_b128 v112, v[34:37]
	v_cvt_pkrtz_f16_f32 v34, v38, v39
	v_cvt_pkrtz_f16_f32 v35, v40, v41
	v_cvt_pkrtz_f16_f32 v36, v42, v43
	v_cvt_pkrtz_f16_f32 v37, v44, v45
	ds_write_b128 v112, v[34:37] offset:32
	ds_read_b128 v[34:37], v125 offset:20480
	v_fmamk_f32 v60, v196, 0x3e38aa3b, v4
	v_fmamk_f32 v61, v197, 0x3e38aa3b, v5
	ds_read_b128 v[2:5], v125 offset:21504
	s_waitcnt lgkmcnt(0)
	v_mfma_f32_32x32x16_f16 v[34:49], v[50:53], v[34:37], 0
	v_fmamk_f32 v14, v206, 0x3e38aa3b, v14
	v_fmamk_f32 v15, v207, 0x3e38aa3b, v15
	v_fmamk_f32 v16, v208, 0x3e38aa3b, v16
	v_fmac_f32_e32 v17, 0x3e38aa3b, v209
	v_mfma_f32_32x32x16_f16 v[34:49], v[62:65], v[2:5], v[34:49]
	ds_read_b128 v[2:5], v125 offset:22528
	v_mfma_f32_32x32x16_f16 v[18:33], v[178:181], v[50:53], 0
	v_fmamk_f32 v50, v199, 0x3e38aa3b, v7
	v_fmamk_f32 v51, v200, 0x3e38aa3b, v8
	v_fmamk_f32 v52, v201, 0x3e38aa3b, v9
	ds_read_b128 v[6:9], v125 offset:23552
	s_waitcnt lgkmcnt(0)
	v_mfma_f32_32x32x16_f16 v[34:49], v[78:81], v[2:5], v[34:49]
	v_add3_u32 v2, s0, v169, v160
	ds_read_b32 v2, v2 offset:16256
	s_lshl_b32 s0, s28, 9
	s_add_i32 s0, s0, 0
	s_add_i32 s14, s0, 0x27800
	v_mfma_f32_32x32x16_f16 v[18:33], v[182:185], v[62:65], v[18:33]
	v_mfma_f32_32x32x16_f16 v[34:49], v[114:117], v[6:9], v[34:49]
	v_mfma_f32_32x32x16_f16 v[18:33], v[186:189], v[78:81], v[18:33]
	s_waitcnt lgkmcnt(0)
	s_nop 9
	v_add_f32_e32 v3, v2, v34
	v_add_f32_e32 v4, v2, v35
	v_add_f32_e32 v5, v2, v36
	v_add_f32_e32 v6, v2, v37
	v_add_f32_e32 v7, v2, v38
	v_add_f32_e32 v8, v2, v39
	v_add_f32_e32 v9, v2, v40
	v_add_f32_e32 v10, v2, v41
	v_add_f32_e32 v11, v2, v42
	v_add_f32_e32 v12, v2, v43
	v_add_f32_e32 v13, v2, v44
	v_add_f32_e32 v34, v2, v45
	v_add_f32_e32 v35, v2, v46
	v_add_f32_e32 v36, v2, v47
	v_add_f32_e32 v37, v2, v48
	v_add_f32_e32 v38, v2, v49
	v_cvt_pkrtz_f16_f32 v2, v3, v4
	v_cvt_pkrtz_f16_f32 v3, v5, v6
	v_cvt_pkrtz_f16_f32 v4, v7, v8
	v_cvt_pkrtz_f16_f32 v5, v9, v10
	ds_write_b128 v112, v[2:5] offset:8704
	v_cvt_pkrtz_f16_f32 v2, v11, v12
	v_cvt_pkrtz_f16_f32 v3, v13, v34
	v_cvt_pkrtz_f16_f32 v4, v35, v36
	v_cvt_pkrtz_f16_f32 v5, v37, v38
	ds_write_b128 v112, v[2:5] offset:8736
	s_nop 0
	s_waitcnt lgkmcnt(0)
	s_barrier
	ds_read_b128 v[2:5], v159
	ds_read_b128 v[10:13], v159 offset:32
	v_mfma_f32_32x32x16_f16 v[18:33], v[190:193], v[114:117], v[18:33]
	v_cvt_pkrtz_f16_f32 v6, v58, v59
	v_cvt_pkrtz_f16_f32 v7, v60, v61
	v_cvt_pkrtz_f16_f32 v8, v99, v50
	v_cvt_pkrtz_f16_f32 v9, v51, v52
	v_cvt_pkrtz_f16_f32 v78, v113, v120
	v_cvt_pkrtz_f16_f32 v79, v121, v122
	v_cvt_pkrtz_f16_f32 v80, v14, v15
	s_nop 4
	v_fmamk_f32 v22, v54, 0x3e38aa3b, v22
	v_fmamk_f32 v23, v55, 0x3e38aa3b, v23
	v_fmamk_f32 v24, v56, 0x3e38aa3b, v24
	v_fmamk_f32 v25, v57, 0x3e38aa3b, v25
	s_waitcnt lgkmcnt(1)
	v_mfma_f32_32x32x16_f16 v[50:65], v[2:5], v[6:9], 0
	v_cvt_pkrtz_f16_f32 v81, v16, v17
	ds_read_b128 v[2:5], v159 offset:64
	v_fmamk_f32 v18, v210, 0x3e38aa3b, v18
	v_fmamk_f32 v19, v211, 0x3e38aa3b, v19
	v_fmamk_f32 v20, v212, 0x3e38aa3b, v20
	v_fmamk_f32 v21, v213, 0x3e38aa3b, v21
	v_fmamk_f32 v26, v70, 0x3e38aa3b, v26
	s_waitcnt lgkmcnt(1)
	v_mfma_f32_32x32x16_f16 v[50:65], v[10:13], v[78:81], v[50:65]
	v_fmamk_f32 v27, v71, 0x3e38aa3b, v27
	v_fmamk_f32 v28, v72, 0x3e38aa3b, v28
	v_fmamk_f32 v14, v73, 0x3e38aa3b, v29
	v_cvt_pkrtz_f16_f32 v70, v18, v19
	v_cvt_pkrtz_f16_f32 v71, v20, v21
	v_cvt_pkrtz_f16_f32 v72, v22, v23
	v_cvt_pkrtz_f16_f32 v73, v24, v25
	ds_read_b128 v[10:13], v159 offset:96
	v_fmamk_f32 v15, v66, 0x3e38aa3b, v30
	s_waitcnt lgkmcnt(1)
	v_mfma_f32_32x32x16_f16 v[50:65], v[2:5], v[70:73], v[50:65]
	v_fmamk_f32 v2, v67, 0x3e38aa3b, v31
	v_fmamk_f32 v3, v68, 0x3e38aa3b, v32
	v_fmac_f32_e32 v33, 0x3e38aa3b, v69
	v_cvt_pkrtz_f16_f32 v66, v26, v27
	v_cvt_pkrtz_f16_f32 v67, v28, v14
	v_cvt_pkrtz_f16_f32 v68, v15, v2
	v_cvt_pkrtz_f16_f32 v69, v3, v33
	v_add_u32_e32 v113, v163, v162
	s_waitcnt lgkmcnt(0)
	v_mfma_f32_32x32x16_f16 v[50:65], v[10:13], v[66:69], v[50:65]
	ds_read_b128 v[2:5], v159 offset:4608
	ds_read_b128 v[10:13], v159 offset:4640
	s_waitcnt lgkmcnt(1)
	v_mfma_f32_32x32x16_f16 v[34:49], v[2:5], v[6:9], 0
	s_waitcnt lgkmcnt(0)
	v_mfma_f32_32x32x16_f16 v[34:49], v[10:13], v[78:81], v[34:49]
	ds_read_b128 v[2:5], v159 offset:4672
	ds_read_b128 v[10:13], v159 offset:4704
	s_waitcnt lgkmcnt(1)
	v_mfma_f32_32x32x16_f16 v[34:49], v[2:5], v[70:73], v[34:49]
	s_waitcnt lgkmcnt(0)
	v_mfma_f32_32x32x16_f16 v[34:49], v[10:13], v[66:69], v[34:49]
	ds_read_b128 v[2:5], v159 offset:9216
	ds_read_b128 v[10:13], v159 offset:9248
	s_waitcnt lgkmcnt(1)
	v_mfma_f32_32x32x16_f16 v[18:33], v[2:5], v[6:9], 0
	s_waitcnt lgkmcnt(0)
	v_mfma_f32_32x32x16_f16 v[18:33], v[10:13], v[78:81], v[18:33]
	ds_read_b128 v[2:5], v159 offset:9280
	ds_read_b128 v[10:13], v159 offset:9312
	s_waitcnt lgkmcnt(1)
	v_mfma_f32_32x32x16_f16 v[18:33], v[2:5], v[70:73], v[18:33]
	ds_read_b128 v[2:5], v159 offset:13824
	ds_read_b128 v[114:117], v159 offset:13856
	ds_read_b128 v[120:123], v159 offset:13888
	ds_read_b128 v[164:167], v159 offset:13920
	s_waitcnt lgkmcnt(4)
	v_mfma_f32_32x32x16_f16 v[18:33], v[10:13], v[66:69], v[18:33]
	s_waitcnt lgkmcnt(3)
	v_mfma_f32_32x32x16_f16 v[2:17], v[2:5], v[6:9], 0
	s_waitcnt lgkmcnt(2)
	v_mfma_f32_32x32x16_f16 v[2:17], v[114:117], v[78:81], v[2:17]
	s_waitcnt lgkmcnt(1)
	v_mfma_f32_32x32x16_f16 v[2:17], v[120:123], v[70:73], v[2:17]
	s_waitcnt lgkmcnt(0)
	v_mfma_f32_32x32x16_f16 v[2:17], v[164:167], v[66:69], v[2:17]
	v_mov_b32_e32 v99, 0
	s_nop 10
	s_nop 1
	v_exp_f32_e32 v34, v34
	v_exp_f32_e32 v35, v35
	v_exp_f32_e32 v36, v36
	v_exp_f32_e32 v37, v37
	v_cvt_pkrtz_f16_f32 v34, v34, v35
	v_cvt_pkrtz_f16_f32 v35, v36, v37
	v_exp_f32_e32 v36, v38
	v_exp_f32_e32 v37, v39
	v_exp_f32_e32 v38, v40
	v_exp_f32_e32 v39, v41
	v_exp_f32_e32 v40, v42
	v_exp_f32_e32 v41, v43
	v_exp_f32_e32 v42, v44
	v_exp_f32_e32 v43, v45
	v_cvt_pkrtz_f16_f32 v36, v36, v37
	v_cvt_pkrtz_f16_f32 v37, v38, v39
	v_cvt_pkrtz_f16_f32 v38, v40, v41
	v_cvt_pkrtz_f16_f32 v39, v42, v43
	v_exp_f32_e32 v40, v46
	v_exp_f32_e32 v41, v47
	v_exp_f32_e32 v42, v48
	v_exp_f32_e32 v43, v49
	v_exp_f32_e32 v18, v18
	v_exp_f32_e32 v19, v19
	v_exp_f32_e32 v20, v20
	v_exp_f32_e32 v21, v21
	v_exp_f32_e32 v50, v50
	v_exp_f32_e32 v51, v51
	v_exp_f32_e32 v52, v52
	v_exp_f32_e32 v53, v53
	v_cvt_pkrtz_f16_f32 v40, v40, v41
	v_cvt_pkrtz_f16_f32 v41, v42, v43
	v_cvt_pkrtz_f16_f32 v42, v18, v19
	v_cvt_pkrtz_f16_f32 v43, v20, v21
	v_exp_f32_e32 v18, v22
	v_exp_f32_e32 v19, v23
	v_exp_f32_e32 v20, v24
	v_exp_f32_e32 v21, v25
	v_cvt_pkrtz_f16_f32 v50, v50, v51
	v_cvt_pkrtz_f16_f32 v51, v52, v53
	v_exp_f32_e32 v52, v54
	v_exp_f32_e32 v53, v55
	v_exp_f32_e32 v54, v56
	v_exp_f32_e32 v55, v57
	v_exp_f32_e32 v56, v58
	v_exp_f32_e32 v57, v59
	v_exp_f32_e32 v58, v60
	v_exp_f32_e32 v59, v61
	v_cvt_pkrtz_f16_f32 v44, v18, v19
	v_cvt_pkrtz_f16_f32 v45, v20, v21
	ds_read_b128 v[18:21], v113
	v_exp_f32_e32 v22, v26
	v_exp_f32_e32 v23, v27
	v_cvt_pkrtz_f16_f32 v52, v52, v53
	v_cvt_pkrtz_f16_f32 v53, v54, v55
	v_cvt_pkrtz_f16_f32 v54, v56, v57
	v_cvt_pkrtz_f16_f32 v55, v58, v59
	v_exp_f32_e32 v56, v62
	v_exp_f32_e32 v57, v63
	v_exp_f32_e32 v58, v64
	v_exp_f32_e32 v59, v65
	v_exp_f32_e32 v24, v28
	v_exp_f32_e32 v25, v29
	v_cvt_pkrtz_f16_f32 v46, v22, v23
	v_exp_f32_e32 v48, v30
	v_exp_f32_e32 v49, v31
	v_cvt_pkrtz_f16_f32 v56, v56, v57
	v_cvt_pkrtz_f16_f32 v57, v58, v59
	v_exp_f32_e32 v62, v32
	ds_read_b128 v[58:61], v113 offset:32
	v_cvt_pkrtz_f16_f32 v47, v24, v25
	v_exp_f32_e32 v63, v33
	s_waitcnt lgkmcnt(1)
	v_mfma_f32_32x32x16_f16 v[18:33], v[18:21], v[50:53], 0
	v_cvt_pkrtz_f16_f32 v48, v48, v49
	v_cvt_pkrtz_f16_f32 v49, v62, v63
	ds_read_b128 v[62:65], v113 offset:64
	v_exp_f32_e32 v67, v2
	v_exp_f32_e32 v68, v3
	s_waitcnt lgkmcnt(1)
	v_mfma_f32_32x32x16_f16 v[18:33], v[58:61], v[54:57], v[18:33]
	v_exp_f32_e32 v59, v4
	v_exp_f32_e32 v60, v5
	v_exp_f32_e32 v61, v6
	ds_read_b128 v[2:5], v113 offset:96
	s_waitcnt lgkmcnt(1)
	v_mfma_f32_32x32x16_f16 v[18:33], v[62:65], v[34:37], v[18:33]
	v_exp_f32_e32 v62, v7
	v_exp_f32_e32 v63, v8
	v_exp_f32_e32 v64, v9
	ds_read_b128 v[6:9], v113 offset:128
	s_waitcnt lgkmcnt(1)
	v_mfma_f32_32x32x16_f16 v[18:33], v[2:5], v[38:41], v[18:33]
	v_exp_f32_e32 v10, v10
	ds_read_b128 v[2:5], v113 offset:160
	v_cvt_pkrtz_f16_f32 v58, v67, v68
	v_cvt_pkrtz_f16_f32 v59, v59, v60
	v_cvt_pkrtz_f16_f32 v60, v61, v62
	v_cvt_pkrtz_f16_f32 v61, v63, v64
	s_waitcnt lgkmcnt(1)
	v_mfma_f32_32x32x16_f16 v[18:33], v[6:9], v[42:45], v[18:33]
	v_exp_f32_e32 v11, v11
	v_exp_f32_e32 v12, v12
	v_exp_f32_e32 v13, v13
	ds_read_b128 v[6:9], v113 offset:192
	s_waitcnt lgkmcnt(1)
	v_mfma_f32_32x32x16_f16 v[18:33], v[2:5], v[46:49], v[18:33]
	v_exp_f32_e32 v14, v14
	v_exp_f32_e32 v15, v15
	v_exp_f32_e32 v16, v16
	ds_read_b128 v[2:5], v113 offset:224
	s_waitcnt lgkmcnt(1)
	v_mfma_f32_32x32x16_f16 v[18:33], v[6:9], v[58:61], v[18:33]
	v_exp_f32_e32 v6, v17
	v_cvt_pkrtz_f16_f32 v62, v10, v11
	v_cvt_pkrtz_f16_f32 v63, v12, v13
	v_cvt_pkrtz_f16_f32 v64, v14, v15
	v_cvt_pkrtz_f16_f32 v65, v16, v6
	ds_read_b128 v[6:9], v113 offset:8704
	ds_read_b128 v[66:69], v113 offset:8736
	s_waitcnt lgkmcnt(2)
	v_mfma_f32_32x32x16_f16 v[18:33], v[2:5], v[62:65], v[18:33]
	v_mov_b32_e32 v70, 0
	v_dot2c_f32_f16_e32 v70, 0x3c003c00, v50
	v_dot2c_f32_f16_e32 v70, 0x3c003c00, v51
	v_dot2c_f32_f16_e32 v70, 0x3c003c00, v52
	v_dot2c_f32_f16_e32 v70, 0x3c003c00, v53
	v_dot2c_f32_f16_e32 v70, 0x3c003c00, v54
	v_dot2c_f32_f16_e32 v70, 0x3c003c00, v55
	s_waitcnt lgkmcnt(1)
	v_mfma_f32_32x32x16_f16 v[2:17], v[6:9], v[50:53], 0
	ds_read_b128 v[50:53], v113 offset:8768
	v_dot2c_f32_f16_e32 v70, 0x3c003c00, v56
	v_dot2c_f32_f16_e32 v70, 0x3c003c00, v57
	v_dot2c_f32_f16_e32 v70, 0x3c003c00, v34
	v_dot2c_f32_f16_e32 v70, 0x3c003c00, v35
	v_dot2c_f32_f16_e32 v70, 0x3c003c00, v36
	v_dot2c_f32_f16_e32 v70, 0x3c003c00, v37
	s_waitcnt lgkmcnt(1)
	v_mfma_f32_32x32x16_f16 v[2:17], v[66:69], v[54:57], v[2:17]
	ds_read_b128 v[54:57], v113 offset:8800
	v_dot2c_f32_f16_e32 v70, 0x3c003c00, v38
	v_dot2c_f32_f16_e32 v70, 0x3c003c00, v39
	v_dot2c_f32_f16_e32 v70, 0x3c003c00, v40
	v_dot2c_f32_f16_e32 v70, 0x3c003c00, v41
	v_dot2c_f32_f16_e32 v70, 0x3c003c00, v42
	v_dot2c_f32_f16_e32 v70, 0x3c003c00, v43
	s_waitcnt lgkmcnt(1)
	v_mfma_f32_32x32x16_f16 v[2:17], v[50:53], v[34:37], v[2:17]
	v_dot2c_f32_f16_e32 v70, 0x3c003c00, v44
	ds_read_b128 v[34:37], v113 offset:8832
	v_dot2c_f32_f16_e32 v70, 0x3c003c00, v45
	v_dot2c_f32_f16_e32 v70, 0x3c003c00, v46
	v_dot2c_f32_f16_e32 v70, 0x3c003c00, v47
	v_dot2c_f32_f16_e32 v70, 0x3c003c00, v48
	v_dot2c_f32_f16_e32 v70, 0x3c003c00, v49
	s_waitcnt lgkmcnt(1)
	v_mfma_f32_32x32x16_f16 v[2:17], v[54:57], v[38:41], v[2:17]
	v_dot2c_f32_f16_e32 v70, 0x3c003c00, v58
	v_dot2c_f32_f16_e32 v70, 0x3c003c00, v59
	v_dot2c_f32_f16_e32 v70, 0x3c003c00, v60
	ds_read_b128 v[38:41], v113 offset:8864
	v_dot2c_f32_f16_e32 v70, 0x3c003c00, v61
	v_dot2c_f32_f16_e32 v70, 0x3c003c00, v62
	v_dot2c_f32_f16_e32 v70, 0x3c003c00, v63
	s_waitcnt lgkmcnt(1)
	v_mfma_f32_32x32x16_f16 v[2:17], v[34:37], v[42:45], v[2:17]
	v_dot2c_f32_f16_e32 v70, 0x3c003c00, v64
	v_dot2c_f32_f16_e32 v70, 0x3c003c00, v65
	s_nop 2
	v_mov_b32_e32 v34, v70
	v_mov_b32_e32 v35, v70
	s_nop 1
	v_permlane32_swap_b32_e32 v34, v35
	v_cndmask_b32_e64 v42, v34, v35, s[2:3]
	ds_read_b128 v[34:37], v113 offset:8896
	s_waitcnt lgkmcnt(1)
	v_mfma_f32_32x32x16_f16 v[2:17], v[38:41], v[46:49], v[2:17]
	v_add_f32_e32 v38, v70, v42
	v_rcp_f32_e32 v42, v38
	ds_read_b128 v[38:41], v113 offset:8928
	v_fma_f32 v78, v42, v18, v74
	v_fma_f32 v79, v42, v19, v75
	v_fma_f32 v80, v42, v20, v76
	v_fma_f32 v81, v42, v21, v77
	s_waitcnt lgkmcnt(1)
	v_mfma_f32_32x32x16_f16 v[2:17], v[34:37], v[58:61], v[2:17]
	v_fma_f32 v82, v42, v22, v82
	v_fma_f32 v83, v42, v23, v83
	v_fma_f32 v84, v42, v24, v84
	v_fma_f32 v85, v42, v25, v85
	v_fma_f32 v86, v42, v26, v86
	v_fma_f32 v87, v42, v27, v87
	v_fma_f32 v88, v42, v28, v88
	v_fma_f32 v89, v42, v29, v89
	v_fma_f32 v72, v42, v30, v94
	v_fma_f32 v73, v42, v31, v95
	v_fma_f32 v74, v42, v32, v110
	v_fma_f32 v75, v42, v33, v111
	s_waitcnt lgkmcnt(0)
	v_mfma_f32_32x32x16_f16 v[2:17], v[38:41], v[62:65], v[2:17]
	s_nop 11
	v_fma_f32 v76, v42, v2, v108
	v_fma_f32 v77, v42, v3, v109
	v_fma_f32 v68, v42, v4, v106
	v_fma_f32 v69, v42, v5, v107
	v_fma_f32 v70, v42, v6, v104
	v_fma_f32 v71, v42, v7, v105
	v_pk_fma_f32 v[58:59], v[42:43], v[8:9], v[100:101] op_sel_hi:[0,1,1]
	v_pk_fma_f32 v[66:67], v[42:43], v[10:11], v[96:97] op_sel_hi:[0,1,1]
	v_pk_fma_f32 v[60:61], v[42:43], v[12:13], v[92:93] op_sel_hi:[0,1,1]
	v_pk_fma_f32 v[62:63], v[42:43], v[14:15], v[90:91] op_sel_hi:[0,1,1]
	v_pk_fma_f32 v[64:65], v[42:43], v[16:17], v[102:103] op_sel_hi:[0,1,1]
	v_lshl_add_u64 v[2:3], v[118:119], 1, s[4:5]
	v_lshl_add_u64 v[2:3], v[2:3], 0, v[98:99]
	v_cvt_pk_f16_f32 v5, v80, v81
	v_cvt_pk_f16_f32 v4, v78, v79
	s_waitcnt vmcnt(0)
	s_barrier
	global_store_dwordx2 v[2:3], v[4:5], off
	v_cvt_pk_f16_f32 v5, v84, v85
	v_cvt_pk_f16_f32 v4, v82, v83
	global_store_dwordx2 v[2:3], v[4:5], off offset:16
	v_cvt_pk_f16_f32 v5, v88, v89
	v_cvt_pk_f16_f32 v4, v86, v87
	global_store_dwordx2 v[2:3], v[4:5], off offset:32
	v_cvt_pk_f16_f32 v5, v74, v75
	v_cvt_pk_f16_f32 v4, v72, v73
	global_store_dwordx2 v[2:3], v[4:5], off offset:48
	v_cvt_pk_f16_f32 v5, v68, v69
	v_cvt_pk_f16_f32 v4, v76, v77
	global_store_dwordx2 v[2:3], v[4:5], off offset:64
	v_cvt_pk_f16_f32 v5, v58, v59
	v_cvt_pk_f16_f32 v4, v70, v71
	global_store_dwordx2 v[2:3], v[4:5], off offset:80
	v_cvt_pk_f16_f32 v5, v60, v61
	v_cvt_pk_f16_f32 v4, v66, v67
	global_store_dwordx2 v[2:3], v[4:5], off offset:96
	v_cvt_pk_f16_f32 v5, v64, v65
	v_cvt_pk_f16_f32 v4, v62, v63
	v_cmp_gt_u32_e64 s[0:1], 32, v124
	v_lshl_add_u32 v91, v126, 2, s14
	v_lshl_add_u32 v93, v1, 2, s14
	v_mov_b32_e32 v240, 0x3e4ccccd
	v_mov_b32_e32 v241, 0x3e4ccccd
	s_mov_b64 s[4:5], -1
	v_mov_b32_e32 v95, v78
	v_mov_b32_e32 v94, v79
	v_mov_b32_e32 v97, v80
	v_mov_b32_e32 v96, v81
	v_mov_b32_e32 v99, v82
	v_mov_b32_e32 v98, v83
	v_mov_b32_e32 v35, v84
	v_mov_b32_e32 v34, v85
	v_mov_b32_e32 v37, v86
	v_mov_b32_e32 v36, v87
	v_mov_b32_e32 v39, v88
	v_mov_b32_e32 v38, v89
	v_mov_b32_e32 v41, v72
	v_mov_b32_e32 v40, v73
	v_mov_b32_e32 v19, v74
	v_mov_b32_e32 v18, v75
	v_mov_b32_e32 v21, v76
	v_mov_b32_e32 v20, v77
	v_mov_b32_e32 v23, v68
	v_mov_b32_e32 v22, v69
	v_mov_b32_e32 v42, v70
	v_mov_b32_e32 v24, v71
	v_mov_b32_e32 v43, v58
	v_mov_b32_e32 v27, v59
	v_mov_b32_e32 v26, v66
	v_mov_b32_e32 v25, v67
	v_mov_b32_e32 v29, v60
	v_mov_b32_e32 v28, v61
	v_mov_b32_e32 v32, v62
	v_mov_b32_e32 v30, v63
	v_mov_b32_e32 v33, v64
	v_mov_b32_e32 v31, v65
	global_store_dwordx2 v[2:3], v[4:5], off offset:112
	s_branch .LBB2_95
.LBB2_94:
	s_or_b64 exec, exec, s[14:15]
	s_waitcnt lgkmcnt(0)
	s_barrier
	ds_read_b128 v[6:9], v91
	v_cndmask_b32_e64 v3, v4, v5, s[2:3]
	v_add_f32_e32 v10, v2, v3
	ds_read_b128 v[2:5], v91 offset:32
	v_mov_b32_e32 v159, 0
	s_waitcnt lgkmcnt(1)
	v_pk_add_f32 v[238:239], v[10:11], v[6:7] op_sel_hi:[0,1]
	v_pk_mul_f32 v[236:237], v[238:239], v[240:241]
	v_max_f32_e32 v11, v238, v236
	v_max_f32_e32 v12, v239, v237
	v_pk_add_f32 v[242:243], v[10:11], v[8:9] op_sel_hi:[0,1]
	v_pk_mul_f32 v[244:245], v[242:243], v[240:241]
	v_max_f32_e32 v13, v242, v244
	v_max_f32_e32 v14, v243, v245
	s_waitcnt lgkmcnt(0)
	v_pk_add_f32 v[238:239], v[10:11], v[2:3] op_sel_hi:[0,1]
	v_pk_mul_f32 v[236:237], v[238:239], v[240:241]
	v_max_f32_e32 v15, v238, v236
	v_max_f32_e32 v16, v239, v237
	ds_read_b128 v[6:9], v91 offset:64
	v_pk_add_f32 v[242:243], v[10:11], v[4:5] op_sel_hi:[0,1]
	v_pk_mul_f32 v[244:245], v[242:243], v[240:241]
	v_max_f32_e32 v17, v242, v244
	v_max_f32_e32 v20, v243, v245
	ds_read_b128 v[2:5], v91 offset:96
	s_waitcnt lgkmcnt(1)
	v_pk_add_f32 v[238:239], v[10:11], v[6:7] op_sel_hi:[0,1]
	v_pk_mul_f32 v[236:237], v[238:239], v[240:241]
	v_max_f32_e32 v22, v238, v236
	v_max_f32_e32 v23, v239, v237
	v_pk_add_f32 v[242:243], v[10:11], v[8:9] op_sel_hi:[0,1]
	v_pk_mul_f32 v[244:245], v[242:243], v[240:241]
	v_max_f32_e32 v24, v242, v244
	v_max_f32_e32 v25, v243, v245
	s_waitcnt lgkmcnt(0)
	v_pk_add_f32 v[238:239], v[10:11], v[2:3] op_sel_hi:[0,1]
	v_pk_mul_f32 v[236:237], v[238:239], v[240:241]
	v_max_f32_e32 v26, v238, v236
	v_max_f32_e32 v27, v239, v237
	ds_read_b128 v[6:9], v91 offset:128
	v_pk_add_f32 v[242:243], v[10:11], v[4:5] op_sel_hi:[0,1]
	v_pk_mul_f32 v[244:245], v[242:243], v[240:241]
	v_max_f32_e32 v28, v242, v244
	v_max_f32_e32 v29, v243, v245
	ds_read_b128 v[2:5], v91 offset:160
	s_waitcnt lgkmcnt(1)
	v_pk_add_f32 v[238:239], v[10:11], v[6:7] op_sel_hi:[0,1]
	v_pk_mul_f32 v[236:237], v[238:239], v[240:241]
	v_max_f32_e32 v30, v238, v236
	v_max_f32_e32 v31, v239, v237
	v_pk_add_f32 v[242:243], v[10:11], v[8:9] op_sel_hi:[0,1]
	v_pk_mul_f32 v[244:245], v[242:243], v[240:241]
	v_max_f32_e32 v32, v242, v244
	v_max_f32_e32 v33, v243, v245
	s_waitcnt lgkmcnt(0)
	v_pk_add_f32 v[238:239], v[10:11], v[2:3] op_sel_hi:[0,1]
	v_pk_mul_f32 v[236:237], v[238:239], v[240:241]
	v_max_f32_e32 v40, v238, v236
	v_max_f32_e32 v41, v239, v237
	ds_read_b128 v[6:9], v91 offset:192
	v_pk_add_f32 v[242:243], v[10:11], v[4:5] op_sel_hi:[0,1]
	v_pk_mul_f32 v[244:245], v[242:243], v[240:241]
	v_max_f32_e32 v42, v242, v244
	v_max_f32_e32 v43, v243, v245
	ds_read_b128 v[2:5], v91 offset:224
	s_waitcnt lgkmcnt(1)
	v_pk_add_f32 v[238:239], v[10:11], v[6:7] op_sel_hi:[0,1]
	v_pk_mul_f32 v[236:237], v[238:239], v[240:241]
	v_max_f32_e32 v44, v238, v236
	v_max_f32_e32 v45, v239, v237
	v_pk_add_f32 v[242:243], v[10:11], v[8:9] op_sel_hi:[0,1]
	v_pk_mul_f32 v[244:245], v[242:243], v[240:241]
	v_max_f32_e32 v46, v242, v244
	v_max_f32_e32 v47, v243, v245
	s_waitcnt lgkmcnt(0)
	v_pk_add_f32 v[238:239], v[10:11], v[2:3] op_sel_hi:[0,1]
	v_pk_mul_f32 v[236:237], v[238:239], v[240:241]
	v_max_f32_e32 v48, v238, v236
	v_max_f32_e32 v49, v239, v237
	ds_read_b128 v[6:9], v91 offset:256
	v_pk_add_f32 v[242:243], v[10:11], v[4:5] op_sel_hi:[0,1]
	v_pk_mul_f32 v[244:245], v[242:243], v[240:241]
	v_max_f32_e32 v50, v242, v244
	v_max_f32_e32 v51, v243, v245
	ds_read_b128 v[2:5], v91 offset:288
	s_waitcnt lgkmcnt(1)
	v_pk_add_f32 v[238:239], v[10:11], v[6:7] op_sel_hi:[0,1]
	v_pk_mul_f32 v[236:237], v[238:239], v[240:241]
	v_max_f32_e32 v52, v238, v236
	v_max_f32_e32 v53, v239, v237
	v_pk_add_f32 v[242:243], v[10:11], v[8:9] op_sel_hi:[0,1]
	v_pk_mul_f32 v[244:245], v[242:243], v[240:241]
	v_max_f32_e32 v54, v242, v244
	v_max_f32_e32 v55, v243, v245
	s_waitcnt lgkmcnt(0)
	v_pk_add_f32 v[238:239], v[10:11], v[2:3] op_sel_hi:[0,1]
	v_pk_mul_f32 v[236:237], v[238:239], v[240:241]
	v_max_f32_e32 v56, v238, v236
	v_max_f32_e32 v57, v239, v237
	ds_read_b128 v[6:9], v91 offset:320
	v_pk_add_f32 v[242:243], v[10:11], v[4:5] op_sel_hi:[0,1]
	v_pk_mul_f32 v[244:245], v[242:243], v[240:241]
	v_max_f32_e32 v92, v242, v244
	v_max_f32_e32 v94, v243, v245
	ds_read_b128 v[2:5], v91 offset:352
	s_waitcnt lgkmcnt(1)
	v_pk_add_f32 v[238:239], v[10:11], v[6:7] op_sel_hi:[0,1]
	v_pk_mul_f32 v[236:237], v[238:239], v[240:241]
	v_max_f32_e32 v95, v238, v236
	v_max_f32_e32 v96, v239, v237
	v_pk_add_f32 v[242:243], v[10:11], v[8:9] op_sel_hi:[0,1]
	v_pk_mul_f32 v[244:245], v[242:243], v[240:241]
	v_max_f32_e32 v97, v242, v244
	v_max_f32_e32 v98, v243, v245
	s_waitcnt lgkmcnt(0)
	v_pk_add_f32 v[238:239], v[10:11], v[2:3] op_sel_hi:[0,1]
	v_pk_mul_f32 v[236:237], v[238:239], v[240:241]
	v_max_f32_e32 v99, v238, v236
	v_max_f32_e32 v100, v239, v237
	ds_read_b128 v[6:9], v91 offset:384
	v_pk_add_f32 v[242:243], v[10:11], v[4:5] op_sel_hi:[0,1]
	v_pk_mul_f32 v[244:245], v[242:243], v[240:241]
	v_max_f32_e32 v101, v242, v244
	v_max_f32_e32 v102, v243, v245
	ds_read_b128 v[2:5], v91 offset:416
	s_waitcnt lgkmcnt(1)
	v_pk_add_f32 v[238:239], v[10:11], v[6:7] op_sel_hi:[0,1]
	v_pk_mul_f32 v[236:237], v[238:239], v[240:241]
	v_max_f32_e32 v103, v238, v236
	v_max_f32_e32 v104, v239, v237
	v_pk_add_f32 v[242:243], v[10:11], v[8:9] op_sel_hi:[0,1]
	v_pk_mul_f32 v[244:245], v[242:243], v[240:241]
	v_max_f32_e32 v105, v242, v244
	v_max_f32_e32 v106, v243, v245
	s_waitcnt lgkmcnt(0)
	v_pk_add_f32 v[238:239], v[10:11], v[2:3] op_sel_hi:[0,1]
	v_pk_mul_f32 v[236:237], v[238:239], v[240:241]
	v_max_f32_e32 v107, v238, v236
	v_max_f32_e32 v108, v239, v237
	ds_read_b128 v[6:9], v91 offset:448
	v_pk_add_f32 v[242:243], v[10:11], v[4:5] op_sel_hi:[0,1]
	v_pk_mul_f32 v[244:245], v[242:243], v[240:241]
	v_max_f32_e32 v109, v242, v244
	v_max_f32_e32 v110, v243, v245
	ds_read_b128 v[2:5], v91 offset:480
	s_waitcnt lgkmcnt(1)
	v_pk_add_f32 v[238:239], v[10:11], v[6:7] op_sel_hi:[0,1]
	v_pk_mul_f32 v[236:237], v[238:239], v[240:241]
	v_max_f32_e32 v111, v238, v236
	v_max_f32_e32 v114, v239, v237
	v_pk_add_f32 v[242:243], v[10:11], v[8:9] op_sel_hi:[0,1]
	v_pk_mul_f32 v[244:245], v[242:243], v[240:241]
	v_max_f32_e32 v115, v242, v244
	v_max_f32_e32 v116, v243, v245
	s_waitcnt lgkmcnt(0)
	v_pk_add_f32 v[238:239], v[10:11], v[2:3] op_sel_hi:[0,1]
	v_pk_mul_f32 v[236:237], v[238:239], v[240:241]
	v_max_f32_e32 v117, v238, v236
	v_max_f32_e32 v120, v239, v237
	v_pk_add_f32 v[242:243], v[10:11], v[4:5] op_sel_hi:[0,1]
	v_pk_mul_f32 v[244:245], v[242:243], v[240:241]
	v_max_f32_e32 v121, v242, v244
	v_max_f32_e32 v122, v243, v245
	s_nop 1
	v_exp_f32_e32 v2, v11
	v_exp_f32_e32 v3, v12
	v_exp_f32_e32 v4, v14
	v_cvt_pkrtz_f16_f32 v2, v2, v3
	v_exp_f32_e32 v3, v13
	v_and_b32_e32 v18, v127, v2
	v_exp_f32_e32 v5, v20
	v_cvt_pkrtz_f16_f32 v2, v3, v4
	v_and_b32_e32 v19, v128, v2
	v_exp_f32_e32 v2, v15
	v_exp_f32_e32 v3, v16
	v_exp_f32_e32 v4, v17
	v_dot2c_f32_f16_e32 v159, 0x3c003c00, v18
	v_cvt_pkrtz_f16_f32 v2, v2, v3
	v_and_b32_e32 v20, v129, v2
	v_cvt_pkrtz_f16_f32 v2, v4, v5
	v_and_b32_e32 v21, v130, v2
	v_exp_f32_e32 v2, v22
	v_exp_f32_e32 v3, v23
	v_exp_f32_e32 v4, v24
	v_exp_f32_e32 v5, v25
	v_cvt_pkrtz_f16_f32 v2, v2, v3
	v_and_b32_e32 v34, v131, v2
	v_cvt_pkrtz_f16_f32 v2, v4, v5
	v_and_b32_e32 v35, v132, v2
	v_exp_f32_e32 v2, v26
	v_exp_f32_e32 v3, v27
	v_exp_f32_e32 v4, v28
	v_exp_f32_e32 v5, v29
	v_cvt_pkrtz_f16_f32 v2, v2, v3
	v_and_b32_e32 v36, v133, v2
	v_cvt_pkrtz_f16_f32 v2, v4, v5
	v_and_b32_e32 v37, v134, v2
	v_exp_f32_e32 v2, v30
	v_exp_f32_e32 v3, v31
	v_exp_f32_e32 v4, v32
	v_exp_f32_e32 v5, v33
	v_cvt_pkrtz_f16_f32 v2, v2, v3
	v_and_b32_e32 v38, v135, v2
	v_cvt_pkrtz_f16_f32 v2, v4, v5
	v_and_b32_e32 v39, v136, v2
	v_exp_f32_e32 v2, v40
	v_exp_f32_e32 v3, v41
	v_exp_f32_e32 v4, v42
	v_exp_f32_e32 v5, v43
	v_cvt_pkrtz_f16_f32 v2, v2, v3
	v_and_b32_e32 v40, v137, v2
	v_cvt_pkrtz_f16_f32 v2, v4, v5
	v_and_b32_e32 v41, v138, v2
	v_exp_f32_e32 v2, v44
	v_exp_f32_e32 v3, v45
	v_exp_f32_e32 v4, v46
	v_exp_f32_e32 v5, v47
	v_cvt_pkrtz_f16_f32 v2, v2, v3
	v_and_b32_e32 v42, v139, v2
	v_cvt_pkrtz_f16_f32 v2, v4, v5
	v_and_b32_e32 v43, v140, v2
	v_exp_f32_e32 v2, v48
	v_exp_f32_e32 v3, v49
	v_exp_f32_e32 v4, v50
	v_exp_f32_e32 v5, v51
	v_cvt_pkrtz_f16_f32 v2, v2, v3
	v_and_b32_e32 v44, v141, v2
	v_cvt_pkrtz_f16_f32 v2, v4, v5
	v_and_b32_e32 v45, v142, v2
	v_exp_f32_e32 v2, v52
	v_exp_f32_e32 v3, v53
	v_exp_f32_e32 v4, v54
	v_exp_f32_e32 v5, v55
	v_cvt_pkrtz_f16_f32 v2, v2, v3
	v_and_b32_e32 v46, v143, v2
	v_cvt_pkrtz_f16_f32 v2, v4, v5
	v_and_b32_e32 v47, v144, v2
	v_exp_f32_e32 v2, v56
	v_exp_f32_e32 v3, v57
	v_exp_f32_e32 v4, v92
	v_exp_f32_e32 v5, v94
	v_cvt_pkrtz_f16_f32 v2, v2, v3
	v_and_b32_e32 v48, v145, v2
	v_cvt_pkrtz_f16_f32 v2, v4, v5
	v_and_b32_e32 v49, v146, v2
	v_exp_f32_e32 v2, v95
	v_exp_f32_e32 v3, v96
	v_exp_f32_e32 v4, v97
	v_exp_f32_e32 v5, v98
	v_cvt_pkrtz_f16_f32 v2, v2, v3
	v_and_b32_e32 v50, v147, v2
	v_cvt_pkrtz_f16_f32 v2, v4, v5
	v_and_b32_e32 v51, v148, v2
	v_exp_f32_e32 v2, v99
	v_exp_f32_e32 v3, v100
	v_exp_f32_e32 v4, v101
	v_exp_f32_e32 v5, v102
	v_cvt_pkrtz_f16_f32 v2, v2, v3
	v_and_b32_e32 v52, v149, v2
	v_cvt_pkrtz_f16_f32 v2, v4, v5
	v_and_b32_e32 v53, v150, v2
	v_exp_f32_e32 v2, v103
	v_exp_f32_e32 v3, v104
	v_exp_f32_e32 v4, v105
	v_exp_f32_e32 v5, v106
	v_cvt_pkrtz_f16_f32 v2, v2, v3
	v_and_b32_e32 v54, v151, v2
	v_exp_f32_e32 v26, v107
	v_cvt_pkrtz_f16_f32 v2, v4, v5
	v_and_b32_e32 v55, v152, v2
	ds_read_b128 v[2:5], v113
	ds_read_b128 v[22:25], v113 offset:32
	v_exp_f32_e32 v27, v108
	v_exp_f32_e32 v28, v109
	s_waitcnt lgkmcnt(1)
	v_mfma_f32_32x32x16_f16 v[2:17], v[2:5], v[18:21], 0
	v_exp_f32_e32 v29, v110
	v_cvt_pkrtz_f16_f32 v26, v26, v27
	v_and_b32_e32 v56, v153, v26
	v_dot2c_f32_f16_e32 v159, 0x3c003c00, v19
	v_cvt_pkrtz_f16_f32 v30, v28, v29
	ds_read_b128 v[26:29], v113 offset:64
	s_waitcnt lgkmcnt(1)
	v_mfma_f32_32x32x16_f16 v[2:17], v[22:25], v[34:37], v[2:17]
	v_and_b32_e32 v57, v154, v30
	v_exp_f32_e32 v30, v111
	v_exp_f32_e32 v31, v114
	ds_read_b128 v[22:25], v113 offset:96
	v_dot2c_f32_f16_e32 v159, 0x3c003c00, v20
	s_waitcnt lgkmcnt(1)
	v_mfma_f32_32x32x16_f16 v[2:17], v[26:29], v[38:41], v[2:17]
	v_cvt_pkrtz_f16_f32 v26, v30, v31
	v_and_b32_e32 v100, v155, v26
	v_exp_f32_e32 v30, v115
	v_exp_f32_e32 v31, v116
	ds_read_b128 v[26:29], v113 offset:128
	s_waitcnt lgkmcnt(1)
	v_mfma_f32_32x32x16_f16 v[2:17], v[22:25], v[42:45], v[2:17]
	v_dot2c_f32_f16_e32 v159, 0x3c003c00, v21
	v_dot2c_f32_f16_e32 v159, 0x3c003c00, v34
	v_dot2c_f32_f16_e32 v159, 0x3c003c00, v35
	v_cvt_pkrtz_f16_f32 v22, v30, v31
	v_dot2c_f32_f16_e32 v159, 0x3c003c00, v36
	v_and_b32_e32 v101, v156, v22
	v_dot2c_f32_f16_e32 v159, 0x3c003c00, v37
	v_exp_f32_e32 v30, v117
	ds_read_b128 v[22:25], v113 offset:160
	v_dot2c_f32_f16_e32 v159, 0x3c003c00, v38
	s_waitcnt lgkmcnt(1)
	v_mfma_f32_32x32x16_f16 v[2:17], v[26:29], v[46:49], v[2:17]
	v_dot2c_f32_f16_e32 v159, 0x3c003c00, v39
	v_dot2c_f32_f16_e32 v159, 0x3c003c00, v40
	v_dot2c_f32_f16_e32 v159, 0x3c003c00, v41
	v_dot2c_f32_f16_e32 v159, 0x3c003c00, v42
	v_dot2c_f32_f16_e32 v159, 0x3c003c00, v43
	v_exp_f32_e32 v31, v120
	v_dot2c_f32_f16_e32 v159, 0x3c003c00, v44
	v_exp_f32_e32 v32, v121
	v_dot2c_f32_f16_e32 v159, 0x3c003c00, v45
	v_exp_f32_e32 v33, v122
	ds_read_b128 v[26:29], v113 offset:192
	v_dot2c_f32_f16_e32 v159, 0x3c003c00, v46
	s_waitcnt lgkmcnt(1)
	v_mfma_f32_32x32x16_f16 v[2:17], v[22:25], v[50:53], v[2:17]
	v_dot2c_f32_f16_e32 v159, 0x3c003c00, v47
	v_dot2c_f32_f16_e32 v159, 0x3c003c00, v48
	v_dot2c_f32_f16_e32 v159, 0x3c003c00, v49
	v_dot2c_f32_f16_e32 v159, 0x3c003c00, v50
	v_dot2c_f32_f16_e32 v159, 0x3c003c00, v51
	v_cvt_pkrtz_f16_f32 v22, v30, v31
	v_dot2c_f32_f16_e32 v159, 0x3c003c00, v52
	v_and_b32_e32 v102, v157, v22
	v_cvt_pkrtz_f16_f32 v22, v32, v33
	v_dot2c_f32_f16_e32 v159, 0x3c003c00, v53
	v_and_b32_e32 v103, v158, v22
	ds_read_b128 v[22:25], v113 offset:224
	v_dot2c_f32_f16_e32 v159, 0x3c003c00, v54
	s_waitcnt lgkmcnt(1)
	v_mfma_f32_32x32x16_f16 v[2:17], v[26:29], v[54:57], v[2:17]
	v_dot2c_f32_f16_e32 v159, 0x3c003c00, v55
	v_dot2c_f32_f16_e32 v159, 0x3c003c00, v56
	v_dot2c_f32_f16_e32 v159, 0x3c003c00, v57
	v_dot2c_f32_f16_e32 v159, 0x3c003c00, v100
	v_dot2c_f32_f16_e32 v159, 0x3c003c00, v101
	v_dot2c_f32_f16_e32 v159, 0x3c003c00, v102
	v_dot2c_f32_f16_e32 v159, 0x3c003c00, v103
	s_waitcnt lgkmcnt(0)
	v_mfma_f32_32x32x16_f16 v[2:17], v[22:25], v[100:103], v[2:17]
	s_xor_b64 s[14:15], s[4:5], -1
	s_mov_b32 s17, 1
	v_mov_b32_e32 v26, v159
	v_mov_b32_e32 v27, v159
	s_nop 1
	v_permlane32_swap_b32_e32 v26, v27
	v_cndmask_b32_e64 v26, v26, v27, s[2:3]
	v_add_f32_e32 v26, v159, v26
	v_rcp_f32_e32 v92, v26
	s_mov_b64 s[4:5], 0
	s_nop 0
	v_pk_mul_f32 v[2:3], v[92:93], v[2:3] op_sel_hi:[0,1]
	v_mul_f32_e32 v22, 0x3fb8aa3b, v2
	v_mul_f32_e32 v23, 0x3fb8aa3b, v3
	v_exp_f32_e32 v22, v22
	v_exp_f32_e32 v23, v23
	v_pk_mul_f32 v[24:25], v[92:93], v[4:5] op_sel_hi:[0,1]
	v_mul_f32_e32 v4, 0x3fb8aa3b, v24
	v_mul_f32_e32 v5, 0x3fb8aa3b, v25
	v_pk_add_f32 v[22:23], v[22:23], -1.0 op_sel_hi:[1,0]
	v_exp_f32_e32 v4, v4
	v_exp_f32_e32 v5, v5
	v_pk_mul_f32 v[104:105], v[92:93], v[6:7] op_sel_hi:[0,1]
	v_pk_mul_f32 v[108:109], v[92:93], v[8:9] op_sel_hi:[0,1]
	v_med3_f32 v94, v3, v23, 0
	v_pk_mul_f32 v[10:11], v[92:93], v[10:11] op_sel_hi:[0,1]
	v_pk_mul_f32 v[12:13], v[92:93], v[12:13] op_sel_hi:[0,1]
	v_med3_f32 v95, v2, v22, 0
	v_mul_f32_e32 v2, 0x3fb8aa3b, v104
	v_exp_f32_e32 v6, v2
	v_mul_f32_e32 v2, 0x3fb8aa3b, v105
	v_pk_add_f32 v[22:23], v[4:5], -1.0 op_sel_hi:[1,0]
	v_exp_f32_e32 v7, v2
	ds_read_b128 v[2:5], v113 offset:8704
	v_pk_mul_f32 v[14:15], v[92:93], v[14:15] op_sel_hi:[0,1]
	v_pk_add_f32 v[106:107], v[6:7], -1.0 op_sel_hi:[1,0]
	v_mul_f32_e32 v6, 0x3fb8aa3b, v108
	v_med3_f32 v96, v25, v23, 0
	v_exp_f32_e32 v110, v6
	ds_read_b128 v[6:9], v113 offset:8736
	v_med3_f32 v97, v24, v22, 0
	s_waitcnt lgkmcnt(1)
	v_mfma_f32_32x32x16_f16 v[18:33], v[2:5], v[18:21], 0
	v_mul_f32_e32 v2, 0x3fb8aa3b, v109
	v_exp_f32_e32 v111, v2
	ds_read_b128 v[2:5], v113 offset:8768
	v_med3_f32 v98, v105, v107, 0
	s_waitcnt lgkmcnt(1)
	v_mfma_f32_32x32x16_f16 v[18:33], v[6:9], v[34:37], v[18:33]
	v_mul_f32_e32 v6, 0x3fb8aa3b, v10
	v_exp_f32_e32 v36, v6
	v_mul_f32_e32 v6, 0x3fb8aa3b, v11
	v_exp_f32_e32 v37, v6
	ds_read_b128 v[6:9], v113 offset:8800
	v_cmp_lt_f32_e32 vcc, 0, v104
	s_waitcnt lgkmcnt(1)
	v_mfma_f32_32x32x16_f16 v[18:33], v[2:5], v[38:41], v[18:33]
	v_mul_f32_e32 v2, 0x3fb8aa3b, v12
	v_exp_f32_e32 v40, v2
	ds_read_b128 v[2:5], v113 offset:8832
	v_add_f32_e32 v38, -1.0, v36
	v_add_f32_e32 v39, -1.0, v37
	v_mul_f32_e32 v36, 0x3fb8aa3b, v13
	v_cndmask_b32_e32 v99, v106, v104, vcc
	v_add_f32_e32 v104, -1.0, v110
	v_add_f32_e32 v105, -1.0, v111
	s_waitcnt lgkmcnt(1)
	v_mfma_f32_32x32x16_f16 v[18:33], v[6:9], v[42:45], v[18:33]
	ds_read_b128 v[6:9], v113 offset:8864
	v_exp_f32_e32 v41, v36
	v_med3_f32 v34, v109, v105, 0
	s_waitcnt lgkmcnt(1)
	v_mfma_f32_32x32x16_f16 v[18:33], v[2:5], v[46:49], v[18:33]
	v_med3_f32 v35, v108, v104, 0
	v_mul_f32_e32 v2, 0x3fb8aa3b, v14
	v_med3_f32 v36, v11, v39, 0
	s_waitcnt lgkmcnt(0)
	v_mfma_f32_32x32x16_f16 v[18:33], v[6:9], v[50:53], v[18:33]
	v_med3_f32 v37, v10, v38, 0
	v_add_f32_e64 v10, v40, -1.0
	v_add_f32_e64 v11, v41, -1.0
	v_exp_f32_e32 v40, v2
	v_mul_f32_e32 v2, 0x3fb8aa3b, v15
	v_exp_f32_e32 v41, v2
	ds_read_b128 v[2:5], v113 offset:8896
	v_med3_f32 v38, v13, v11, 0
	v_med3_f32 v39, v12, v10, 0
	v_pk_mul_f32 v[12:13], v[92:93], v[16:17] op_sel_hi:[0,1]
	v_mul_f32_e32 v6, 0x3fb8aa3b, v12
	v_exp_f32_e32 v16, v6
	ds_read_b128 v[6:9], v113 offset:8928
	s_waitcnt lgkmcnt(1)
	v_mfma_f32_32x32x16_f16 v[18:33], v[2:5], v[54:57], v[18:33]
	v_mul_f32_e32 v2, 0x3fb8aa3b, v13
	v_exp_f32_e32 v17, v2
	v_add_f32_e32 v10, -1.0, v40
	v_add_f32_e32 v11, -1.0, v41
	s_waitcnt lgkmcnt(0)
	v_add_f32_e32 v2, -1.0, v16
	v_add_f32_e32 v3, -1.0, v17
	v_med3_f32 v40, v15, v11, 0
	v_mfma_f32_32x32x16_f16 v[18:33], v[6:9], v[100:103], v[18:33]
	s_barrier
	v_med3_f32 v41, v14, v10, 0
	s_nop 9
	v_pk_mul_f32 v[4:5], v[92:93], v[18:19] op_sel_hi:[0,1]
	v_mul_f32_e32 v6, 0x3fb8aa3b, v4
	v_mul_f32_e32 v7, 0x3fb8aa3b, v5
	v_exp_f32_e32 v6, v6
	v_exp_f32_e32 v7, v7
	s_nop 4
	v_med3_f32 v18, v13, v3, 0
	s_nop 3
	v_med3_f32 v19, v12, v2, 0
	v_pk_add_f32 v[2:3], v[6:7], -1.0 op_sel_hi:[1,0]
	s_nop 1
	v_pk_mul_f32 v[6:7], v[92:93], v[20:21] op_sel_hi:[0,1]
	v_mul_f32_e32 v8, 0x3fb8aa3b, v6
	v_mul_f32_e32 v9, 0x3fb8aa3b, v7
	v_exp_f32_e32 v8, v8
	v_exp_f32_e32 v9, v9
	v_med3_f32 v20, v5, v3, 0
	v_med3_f32 v21, v4, v2, 0
	v_pk_mul_f32 v[4:5], v[92:93], v[22:23] op_sel_hi:[0,1]
	v_pk_add_f32 v[2:3], v[8:9], -1.0 op_sel_hi:[1,0]
	v_mul_f32_e32 v8, 0x3fb8aa3b, v4
	v_mul_f32_e32 v9, 0x3fb8aa3b, v5
	v_exp_f32_e32 v8, v8
	v_exp_f32_e32 v9, v9
	v_med3_f32 v22, v7, v3, 0
	v_med3_f32 v23, v6, v2, 0
	v_pk_mul_f32 v[6:7], v[92:93], v[24:25] op_sel_hi:[0,1]
	v_pk_add_f32 v[2:3], v[8:9], -1.0 op_sel_hi:[1,0]
	v_mul_f32_e32 v8, 0x3fb8aa3b, v6
	v_mul_f32_e32 v9, 0x3fb8aa3b, v7
	v_exp_f32_e32 v8, v8
	v_exp_f32_e32 v9, v9
	v_med3_f32 v24, v5, v3, 0
	v_med3_f32 v42, v4, v2, 0
	v_pk_mul_f32 v[4:5], v[92:93], v[26:27] op_sel_hi:[0,1]
	v_pk_add_f32 v[2:3], v[8:9], -1.0 op_sel_hi:[1,0]
	v_mul_f32_e32 v8, 0x3fb8aa3b, v4
	v_mul_f32_e32 v9, 0x3fb8aa3b, v5
	v_exp_f32_e32 v8, v8
	v_exp_f32_e32 v9, v9
	v_med3_f32 v27, v7, v3, 0
	v_med3_f32 v43, v6, v2, 0
	v_pk_mul_f32 v[6:7], v[92:93], v[28:29] op_sel_hi:[0,1]
	v_pk_add_f32 v[2:3], v[8:9], -1.0 op_sel_hi:[1,0]
	v_mul_f32_e32 v8, 0x3fb8aa3b, v6
	v_mul_f32_e32 v9, 0x3fb8aa3b, v7
	v_exp_f32_e32 v8, v8
	v_exp_f32_e32 v9, v9
	v_med3_f32 v25, v5, v3, 0
	v_med3_f32 v26, v4, v2, 0
	v_pk_mul_f32 v[4:5], v[92:93], v[30:31] op_sel_hi:[0,1]
	v_pk_add_f32 v[2:3], v[8:9], -1.0 op_sel_hi:[1,0]
	v_mul_f32_e32 v8, 0x3fb8aa3b, v4
	v_mul_f32_e32 v9, 0x3fb8aa3b, v5
	v_exp_f32_e32 v8, v8
	v_exp_f32_e32 v9, v9
	v_med3_f32 v28, v7, v3, 0
	v_med3_f32 v29, v6, v2, 0
	v_pk_mul_f32 v[6:7], v[92:93], v[32:33] op_sel_hi:[0,1]
	v_pk_add_f32 v[2:3], v[8:9], -1.0 op_sel_hi:[1,0]
	v_mul_f32_e32 v8, 0x3fb8aa3b, v6
	v_mul_f32_e32 v9, 0x3fb8aa3b, v7
	v_exp_f32_e32 v8, v8
	v_exp_f32_e32 v9, v9
	v_med3_f32 v30, v5, v3, 0
	v_med3_f32 v32, v4, v2, 0
	v_pk_add_f32 v[2:3], v[8:9], -1.0 op_sel_hi:[1,0]
	v_med3_f32 v31, v7, v3, 0
	v_med3_f32 v33, v6, v2, 0
	s_and_b64 vcc, exec, s[14:15]
	s_cbranch_vccnz .LBB2_97
